# t19
# baseline (speedup 1.0000x reference)
_Z11align_fusedPKfS0_PKiPf:
	s_load_dwordx8 s[4:11], s[0:1], 0x0
	s_sub_u32 s2, 0x1fff, s2
	s_mul_i32 s12, s2, 0x5dc0
	v_and_b32_e32 v7, 63, v0
	v_readfirstlane_b32 s13, v0
	v_lshlrev_b32_e32 v1, 4, v7
	v_mul_u32_u24_e32 v3, 12, v7
	s_mul_i32 s18, s13, 96
	s_mul_i32 s3, s13, 6
	s_sub_u32 s3, 0x49c, s3
	v_cmp_gt_u32_e64 s[14:15], s3, v7
	v_add_u32_e32 v2, s18, v1
	v_add_u32_e32 v3, s18, v3
	v_add_u32_e32 v4, 0x600, v3
	s_add_u32 s12, s12, s18
	s_add_u32 s12, s12, 0x800
	s_waitcnt lgkmcnt(0)
	s_sub_u32 s44, s12, 0x800
	s_add_u32 s40, s4, s44
	s_addc_u32 s41, s5, 0
	s_add_u32 s42, s40, 0x1000
	s_addc_u32 s43, s41, 0
	s_add_u32 s4, s4, s12
	s_addc_u32 s5, s5, 0
	s_add_u32 s10, s10, s12
	s_addc_u32 s11, s11, 0
	s_cmp_lg_u32 s13, 0
	s_cbranch_scc1 .Lbulk_waves
	v_lshlrev_b32_e32 v5, 2, v7
	global_load_dword v5, v5, s[8:9]
	global_load_dwordx3 v[44:46], v3, s[6:7] nt
	s_mov_b32 m0, s18
	s_nop 0
	global_load_lds_dwordx4 v1, s[40:41] nt
	global_load_lds_dwordx4 v1, s[40:41] offset:1024 nt
	global_load_lds_dwordx4 v1, s[40:41] offset:2048 nt
	global_load_lds_dwordx4 v1, s[40:41] offset:3072 nt
	s_add_u32 m0, s18, 0x1000
	s_nop 0
	global_load_lds_dwordx4 v1, s[42:43] nt
	global_load_lds_dwordx4 v1, s[42:43] offset:1024 nt
	s_mov_b32 s20, 0
	s_mov_b32 s21, 0x10000
	s_mov_b32 s22, 0
	s_mov_b32 s23, 0x20000
	s_mov_b32 s24, 0
	s_mov_b32 s25, 0x40000
	s_mov_b32 s26, 0
	s_mov_b32 s27, 0x80000
	s_waitcnt vmcnt(6)
	v_mul_u32_u24_e32 v5, 12, v5
	v_add_f32_dpp v52, v44, v44 quad_perm:[1,0,3,2] row_mask:0xf bank_mask:0xf
	v_add_f32_dpp v53, v45, v45 quad_perm:[1,0,3,2] row_mask:0xf bank_mask:0xf
	v_add_f32_dpp v54, v46, v46 quad_perm:[1,0,3,2] row_mask:0xf bank_mask:0xf
	v_add_f32_dpp v52, v52, v52 quad_perm:[2,3,0,1] row_mask:0xf bank_mask:0xf
	v_add_f32_dpp v53, v53, v53 quad_perm:[2,3,0,1] row_mask:0xf bank_mask:0xf
	v_add_f32_dpp v54, v54, v54 quad_perm:[2,3,0,1] row_mask:0xf bank_mask:0xf
	v_add_f32_dpp v52, v52, v52 row_half_mirror row_mask:0xf bank_mask:0xf
	v_add_f32_dpp v53, v53, v53 row_half_mirror row_mask:0xf bank_mask:0xf
	v_add_f32_dpp v54, v54, v54 row_half_mirror row_mask:0xf bank_mask:0xf
	v_add_f32_dpp v52, v52, v52 row_mirror row_mask:0xf bank_mask:0xf
	v_add_f32_dpp v53, v53, v53 row_mirror row_mask:0xf bank_mask:0xf
	v_add_f32_dpp v54, v54, v54 row_mirror row_mask:0xf bank_mask:0xf
	v_add_f32_dpp v52, v52, v52 row_bcast:15 row_mask:0xa bank_mask:0xf
	v_add_f32_dpp v53, v53, v53 row_bcast:15 row_mask:0xa bank_mask:0xf
	v_add_f32_dpp v54, v54, v54 row_bcast:15 row_mask:0xa bank_mask:0xf
	v_add_f32_dpp v52, v52, v52 row_bcast:31 row_mask:0xc bank_mask:0xf
	v_add_f32_dpp v53, v53, v53 row_bcast:31 row_mask:0xc bank_mask:0xf
	v_add_f32_dpp v54, v54, v54 row_bcast:31 row_mask:0xc bank_mask:0xf
	v_readlane_b32 s28, v52, 63
	v_readlane_b32 s29, v53, 63
	v_readlane_b32 s30, v54, 63
	v_mov_b32_e32 v52, s28
	v_mov_b32_e32 v53, s29
	v_mov_b32_e32 v54, s30
	v_fmac_f32_e32 v44, 0xbc800000, v52
	v_fmac_f32_e32 v45, 0xbc800000, v53
	v_fmac_f32_e32 v46, 0xbc800000, v54
	s_waitcnt vmcnt(0)
	s_waitcnt lgkmcnt(0)
	s_barrier
	ds_read_b32 v48, v5
	ds_read_b32 v49, v5 offset:4
	ds_read_b32 v50, v5 offset:8
	s_waitcnt lgkmcnt(0)
	v_add_f32_dpp v52, v48, v48 quad_perm:[1,0,3,2] row_mask:0xf bank_mask:0xf
	v_add_f32_dpp v53, v49, v49 quad_perm:[1,0,3,2] row_mask:0xf bank_mask:0xf
	v_add_f32_dpp v54, v50, v50 quad_perm:[1,0,3,2] row_mask:0xf bank_mask:0xf
	v_add_f32_dpp v52, v52, v52 quad_perm:[2,3,0,1] row_mask:0xf bank_mask:0xf
	v_add_f32_dpp v53, v53, v53 quad_perm:[2,3,0,1] row_mask:0xf bank_mask:0xf
	v_add_f32_dpp v54, v54, v54 quad_perm:[2,3,0,1] row_mask:0xf bank_mask:0xf
	v_add_f32_dpp v52, v52, v52 row_half_mirror row_mask:0xf bank_mask:0xf
	v_add_f32_dpp v53, v53, v53 row_half_mirror row_mask:0xf bank_mask:0xf
	v_add_f32_dpp v54, v54, v54 row_half_mirror row_mask:0xf bank_mask:0xf
	v_add_f32_dpp v52, v52, v52 row_mirror row_mask:0xf bank_mask:0xf
	v_add_f32_dpp v53, v53, v53 row_mirror row_mask:0xf bank_mask:0xf
	v_add_f32_dpp v54, v54, v54 row_mirror row_mask:0xf bank_mask:0xf
	v_add_f32_dpp v52, v52, v52 row_bcast:15 row_mask:0xa bank_mask:0xf
	v_add_f32_dpp v53, v53, v53 row_bcast:15 row_mask:0xa bank_mask:0xf
	v_add_f32_dpp v54, v54, v54 row_bcast:15 row_mask:0xa bank_mask:0xf
	v_add_f32_dpp v52, v52, v52 row_bcast:31 row_mask:0xc bank_mask:0xf
	v_add_f32_dpp v53, v53, v53 row_bcast:31 row_mask:0xc bank_mask:0xf
	v_add_f32_dpp v54, v54, v54 row_bcast:31 row_mask:0xc bank_mask:0xf
	v_readlane_b32 s32, v52, 63
	v_readlane_b32 s33, v53, 63
	v_readlane_b32 s34, v54, 63
	v_mov_b32_e32 v52, s32
	v_mov_b32_e32 v53, s33
	v_mov_b32_e32 v54, s34
	v_fmac_f32_e32 v48, 0xbc800000, v52
	v_fmac_f32_e32 v49, 0xbc800000, v53
	v_fmac_f32_e32 v50, 0xbc800000, v54
	v_mul_f32_e32 v52, v48, v44
	v_mul_f32_e32 v53, v48, v45
	v_mul_f32_e32 v54, v48, v46
	v_mul_f32_e32 v55, v49, v44
	v_mul_f32_e32 v56, v49, v45
	v_mul_f32_e32 v57, v49, v46
	v_mul_f32_e32 v58, v50, v44
	v_mul_f32_e32 v59, v50, v45
	v_mul_f32_e32 v60, v50, v46
	v_add_f32_dpp v52, v52, v52 quad_perm:[1,0,3,2] row_mask:0xf bank_mask:0xf
	v_add_f32_dpp v53, v53, v53 quad_perm:[1,0,3,2] row_mask:0xf bank_mask:0xf
	v_add_f32_dpp v54, v54, v54 quad_perm:[1,0,3,2] row_mask:0xf bank_mask:0xf
	v_add_f32_dpp v55, v55, v55 quad_perm:[1,0,3,2] row_mask:0xf bank_mask:0xf
	v_add_f32_dpp v56, v56, v56 quad_perm:[1,0,3,2] row_mask:0xf bank_mask:0xf
	v_add_f32_dpp v57, v57, v57 quad_perm:[1,0,3,2] row_mask:0xf bank_mask:0xf
	v_add_f32_dpp v58, v58, v58 quad_perm:[1,0,3,2] row_mask:0xf bank_mask:0xf
	v_add_f32_dpp v59, v59, v59 quad_perm:[1,0,3,2] row_mask:0xf bank_mask:0xf
	v_add_f32_dpp v60, v60, v60 quad_perm:[1,0,3,2] row_mask:0xf bank_mask:0xf
	v_add_f32_dpp v52, v52, v52 quad_perm:[2,3,0,1] row_mask:0xf bank_mask:0xf
	v_add_f32_dpp v53, v53, v53 quad_perm:[2,3,0,1] row_mask:0xf bank_mask:0xf
	v_add_f32_dpp v54, v54, v54 quad_perm:[2,3,0,1] row_mask:0xf bank_mask:0xf
	v_add_f32_dpp v55, v55, v55 quad_perm:[2,3,0,1] row_mask:0xf bank_mask:0xf
	v_add_f32_dpp v56, v56, v56 quad_perm:[2,3,0,1] row_mask:0xf bank_mask:0xf
	v_add_f32_dpp v57, v57, v57 quad_perm:[2,3,0,1] row_mask:0xf bank_mask:0xf
	v_add_f32_dpp v58, v58, v58 quad_perm:[2,3,0,1] row_mask:0xf bank_mask:0xf
	v_add_f32_dpp v59, v59, v59 quad_perm:[2,3,0,1] row_mask:0xf bank_mask:0xf
	v_add_f32_dpp v60, v60, v60 quad_perm:[2,3,0,1] row_mask:0xf bank_mask:0xf
	v_add_f32_dpp v52, v52, v52 row_half_mirror row_mask:0xf bank_mask:0xf
	v_add_f32_dpp v53, v53, v53 row_half_mirror row_mask:0xf bank_mask:0xf
	v_add_f32_dpp v54, v54, v54 row_half_mirror row_mask:0xf bank_mask:0xf
	v_add_f32_dpp v55, v55, v55 row_half_mirror row_mask:0xf bank_mask:0xf
	v_add_f32_dpp v56, v56, v56 row_half_mirror row_mask:0xf bank_mask:0xf
	v_add_f32_dpp v57, v57, v57 row_half_mirror row_mask:0xf bank_mask:0xf
	v_add_f32_dpp v58, v58, v58 row_half_mirror row_mask:0xf bank_mask:0xf
	v_add_f32_dpp v59, v59, v59 row_half_mirror row_mask:0xf bank_mask:0xf
	v_add_f32_dpp v60, v60, v60 row_half_mirror row_mask:0xf bank_mask:0xf
	v_add_f32_dpp v52, v52, v52 row_mirror row_mask:0xf bank_mask:0xf
	v_add_f32_dpp v53, v53, v53 row_mirror row_mask:0xf bank_mask:0xf
	v_add_f32_dpp v54, v54, v54 row_mirror row_mask:0xf bank_mask:0xf
	v_add_f32_dpp v55, v55, v55 row_mirror row_mask:0xf bank_mask:0xf
	v_add_f32_dpp v56, v56, v56 row_mirror row_mask:0xf bank_mask:0xf
	v_add_f32_dpp v57, v57, v57 row_mirror row_mask:0xf bank_mask:0xf
	v_add_f32_dpp v58, v58, v58 row_mirror row_mask:0xf bank_mask:0xf
	v_add_f32_dpp v59, v59, v59 row_mirror row_mask:0xf bank_mask:0xf
	v_add_f32_dpp v60, v60, v60 row_mirror row_mask:0xf bank_mask:0xf
	v_add_f32_dpp v52, v52, v52 row_bcast:15 row_mask:0xa bank_mask:0xf
	v_add_f32_dpp v53, v53, v53 row_bcast:15 row_mask:0xa bank_mask:0xf
	v_add_f32_dpp v54, v54, v54 row_bcast:15 row_mask:0xa bank_mask:0xf
	v_add_f32_dpp v55, v55, v55 row_bcast:15 row_mask:0xa bank_mask:0xf
	v_add_f32_dpp v56, v56, v56 row_bcast:15 row_mask:0xa bank_mask:0xf
	v_add_f32_dpp v57, v57, v57 row_bcast:15 row_mask:0xa bank_mask:0xf
	v_add_f32_dpp v58, v58, v58 row_bcast:15 row_mask:0xa bank_mask:0xf
	v_add_f32_dpp v59, v59, v59 row_bcast:15 row_mask:0xa bank_mask:0xf
	v_add_f32_dpp v60, v60, v60 row_bcast:15 row_mask:0xa bank_mask:0xf
	v_add_f32_dpp v52, v52, v52 row_bcast:31 row_mask:0xc bank_mask:0xf
	v_add_f32_dpp v53, v53, v53 row_bcast:31 row_mask:0xc bank_mask:0xf
	v_add_f32_dpp v54, v54, v54 row_bcast:31 row_mask:0xc bank_mask:0xf
	v_add_f32_dpp v55, v55, v55 row_bcast:31 row_mask:0xc bank_mask:0xf
	v_add_f32_dpp v56, v56, v56 row_bcast:31 row_mask:0xc bank_mask:0xf
	v_add_f32_dpp v57, v57, v57 row_bcast:31 row_mask:0xc bank_mask:0xf
	v_add_f32_dpp v58, v58, v58 row_bcast:31 row_mask:0xc bank_mask:0xf
	v_add_f32_dpp v59, v59, v59 row_bcast:31 row_mask:0xc bank_mask:0xf
	v_add_f32_dpp v60, v60, v60 row_bcast:31 row_mask:0xc bank_mask:0xf
	v_cndmask_b32_e64 v52, v52, v55, s[22:23]
	v_cndmask_b32_e64 v53, v53, v56, s[22:23]
	v_cndmask_b32_e64 v54, v54, v57, s[22:23]
	v_cndmask_b32_e64 v52, v52, v58, s[24:25]
	v_cndmask_b32_e64 v53, v53, v59, s[24:25]
	v_cndmask_b32_e64 v54, v54, v60, s[24:25]
	v_cndmask_b32_e64 v52, v52, 0, s[26:27]
	v_cndmask_b32_e64 v53, v53, 0, s[26:27]
	v_cndmask_b32_e64 v54, v54, 0, s[26:27]
	v_cndmask_b32_e64 v40, 0, 1.0, s[20:21]
	v_cndmask_b32_e64 v41, 0, 1.0, s[22:23]
	v_cndmask_b32_e64 v42, 0, 1.0, s[24:25]
	v_mul_f32_e32 v55, v52, v52
	v_mul_f32_e32 v56, v53, v53
	v_mul_f32_e32 v57, v52, v53
	v_add_f32_dpp v55, v55, v55 quad_perm:[1,0,3,2] row_mask:0xf bank_mask:0xf
	v_add_f32_dpp v56, v56, v56 quad_perm:[1,0,3,2] row_mask:0xf bank_mask:0xf
	v_add_f32_dpp v57, v57, v57 quad_perm:[1,0,3,2] row_mask:0xf bank_mask:0xf
	v_add_f32_dpp v55, v55, v55 quad_perm:[2,3,0,1] row_mask:0xf bank_mask:0xf
	v_add_f32_dpp v56, v56, v56 quad_perm:[2,3,0,1] row_mask:0xf bank_mask:0xf
	v_add_f32_dpp v57, v57, v57 quad_perm:[2,3,0,1] row_mask:0xf bank_mask:0xf
	v_sub_f32_e32 v60, v56, v55
	v_mul_f32_e32 v58, v57, v57
	v_cmp_gt_f32_e32 vcc, 0, v60
	v_mul_f32_e32 v59, v60, v60
	v_fmac_f32_e32 v59, 4.0, v58
	v_sqrt_f32_e32 v59, v59
	s_nop 0
	v_add_f32_e64 v59, |v60|, v59
	v_add_f32_e32 v59, 0x0da24260, v59
	v_rcp_f32_e32 v59, v59
	v_add_f32_e32 v58, v57, v57
	v_mul_f32_e32 v59, v58, v59
	v_cndmask_b32_e64 v59, v59, -v59, vcc
	v_fma_f32 v58, v59, v59, 1.0
	v_rsq_f32_e32 v61, v58
	s_nop 0
	v_mul_f32_e32 v62, v61, v59
	v_mul_f32_e32 v55, v62, v53
	v_mul_f32_e32 v56, v62, v52
	v_fma_f32 v52, v61, v52, -v55
	v_fma_f32 v53, v61, v53, v56
	v_mul_f32_e32 v55, v52, v52
	v_mul_f32_e32 v56, v54, v54
	v_mul_f32_e32 v57, v52, v54
	v_add_f32_dpp v55, v55, v55 quad_perm:[1,0,3,2] row_mask:0xf bank_mask:0xf
	v_add_f32_dpp v56, v56, v56 quad_perm:[1,0,3,2] row_mask:0xf bank_mask:0xf
	v_add_f32_dpp v57, v57, v57 quad_perm:[1,0,3,2] row_mask:0xf bank_mask:0xf
	v_add_f32_dpp v55, v55, v55 quad_perm:[2,3,0,1] row_mask:0xf bank_mask:0xf
	v_add_f32_dpp v56, v56, v56 quad_perm:[2,3,0,1] row_mask:0xf bank_mask:0xf
	v_add_f32_dpp v57, v57, v57 quad_perm:[2,3,0,1] row_mask:0xf bank_mask:0xf
	v_sub_f32_e32 v60, v56, v55
	v_mul_f32_e32 v58, v57, v57
	v_cmp_gt_f32_e32 vcc, 0, v60
	v_mul_f32_e32 v59, v60, v60
	v_fmac_f32_e32 v59, 4.0, v58
	v_sqrt_f32_e32 v59, v59
	v_mul_f32_e32 v63, v62, v41
	v_mul_f32_e32 v43, v62, v40
	v_fma_f32 v40, v61, v40, -v63
	v_fma_f32 v41, v61, v41, v43
	v_add_f32_e64 v59, |v60|, v59
	v_add_f32_e32 v59, 0x0da24260, v59
	v_rcp_f32_e32 v59, v59
	v_add_f32_e32 v58, v57, v57
	v_mul_f32_e32 v59, v58, v59
	v_cndmask_b32_e64 v59, v59, -v59, vcc
	v_fma_f32 v58, v59, v59, 1.0
	v_rsq_f32_e32 v61, v58
	s_nop 0
	v_mul_f32_e32 v62, v61, v59
	v_mul_f32_e32 v55, v62, v54
	v_mul_f32_e32 v56, v62, v52
	v_fma_f32 v52, v61, v52, -v55
	v_fma_f32 v54, v61, v54, v56
	v_mul_f32_e32 v55, v53, v53
	v_mul_f32_e32 v56, v54, v54
	v_mul_f32_e32 v57, v53, v54
	v_add_f32_dpp v55, v55, v55 quad_perm:[1,0,3,2] row_mask:0xf bank_mask:0xf
	v_add_f32_dpp v56, v56, v56 quad_perm:[1,0,3,2] row_mask:0xf bank_mask:0xf
	v_add_f32_dpp v57, v57, v57 quad_perm:[1,0,3,2] row_mask:0xf bank_mask:0xf
	v_add_f32_dpp v55, v55, v55 quad_perm:[2,3,0,1] row_mask:0xf bank_mask:0xf
	v_add_f32_dpp v56, v56, v56 quad_perm:[2,3,0,1] row_mask:0xf bank_mask:0xf
	v_add_f32_dpp v57, v57, v57 quad_perm:[2,3,0,1] row_mask:0xf bank_mask:0xf
	v_sub_f32_e32 v60, v56, v55
	v_mul_f32_e32 v58, v57, v57
	v_cmp_gt_f32_e32 vcc, 0, v60
	v_mul_f32_e32 v59, v60, v60
	v_fmac_f32_e32 v59, 4.0, v58
	v_sqrt_f32_e32 v59, v59
	v_mul_f32_e32 v63, v62, v42
	v_mul_f32_e32 v43, v62, v40
	v_fma_f32 v40, v61, v40, -v63
	v_fma_f32 v42, v61, v42, v43
	v_add_f32_e64 v59, |v60|, v59
	v_add_f32_e32 v59, 0x0da24260, v59
	v_rcp_f32_e32 v59, v59
	v_add_f32_e32 v58, v57, v57
	v_mul_f32_e32 v59, v58, v59
	v_cndmask_b32_e64 v59, v59, -v59, vcc
	v_fma_f32 v58, v59, v59, 1.0
	v_rsq_f32_e32 v61, v58
	s_nop 0
	v_mul_f32_e32 v62, v61, v59
	v_mul_f32_e32 v55, v62, v54
	v_mul_f32_e32 v56, v62, v53
	v_fma_f32 v53, v61, v53, -v55
	v_fma_f32 v54, v61, v54, v56
	v_mul_f32_e32 v55, v52, v52
	v_mul_f32_e32 v56, v53, v53
	v_mul_f32_e32 v57, v52, v53
	v_add_f32_dpp v55, v55, v55 quad_perm:[1,0,3,2] row_mask:0xf bank_mask:0xf
	v_add_f32_dpp v56, v56, v56 quad_perm:[1,0,3,2] row_mask:0xf bank_mask:0xf
	v_add_f32_dpp v57, v57, v57 quad_perm:[1,0,3,2] row_mask:0xf bank_mask:0xf
	v_add_f32_dpp v55, v55, v55 quad_perm:[2,3,0,1] row_mask:0xf bank_mask:0xf
	v_add_f32_dpp v56, v56, v56 quad_perm:[2,3,0,1] row_mask:0xf bank_mask:0xf
	v_add_f32_dpp v57, v57, v57 quad_perm:[2,3,0,1] row_mask:0xf bank_mask:0xf
	v_sub_f32_e32 v60, v56, v55
	v_mul_f32_e32 v58, v57, v57
	v_cmp_gt_f32_e32 vcc, 0, v60
	v_mul_f32_e32 v59, v60, v60
	v_fmac_f32_e32 v59, 4.0, v58
	v_sqrt_f32_e32 v59, v59
	v_mul_f32_e32 v63, v62, v42
	v_mul_f32_e32 v43, v62, v41
	v_fma_f32 v41, v61, v41, -v63
	v_fma_f32 v42, v61, v42, v43
	v_add_f32_e64 v59, |v60|, v59
	v_add_f32_e32 v59, 0x0da24260, v59
	v_rcp_f32_e32 v59, v59
	v_add_f32_e32 v58, v57, v57
	v_mul_f32_e32 v59, v58, v59
	v_cndmask_b32_e64 v59, v59, -v59, vcc
	v_fma_f32 v58, v59, v59, 1.0
	v_rsq_f32_e32 v61, v58
	s_nop 0
	v_mul_f32_e32 v62, v61, v59
	v_mul_f32_e32 v55, v62, v53
	v_mul_f32_e32 v56, v62, v52
	v_fma_f32 v52, v61, v52, -v55
	v_fma_f32 v53, v61, v53, v56
	v_mul_f32_e32 v55, v52, v52
	v_mul_f32_e32 v56, v54, v54
	v_mul_f32_e32 v57, v52, v54
	v_add_f32_dpp v55, v55, v55 quad_perm:[1,0,3,2] row_mask:0xf bank_mask:0xf
	v_add_f32_dpp v56, v56, v56 quad_perm:[1,0,3,2] row_mask:0xf bank_mask:0xf
	v_add_f32_dpp v57, v57, v57 quad_perm:[1,0,3,2] row_mask:0xf bank_mask:0xf
	v_add_f32_dpp v55, v55, v55 quad_perm:[2,3,0,1] row_mask:0xf bank_mask:0xf
	v_add_f32_dpp v56, v56, v56 quad_perm:[2,3,0,1] row_mask:0xf bank_mask:0xf
	v_add_f32_dpp v57, v57, v57 quad_perm:[2,3,0,1] row_mask:0xf bank_mask:0xf
	v_sub_f32_e32 v60, v56, v55
	v_mul_f32_e32 v58, v57, v57
	v_cmp_gt_f32_e32 vcc, 0, v60
	v_mul_f32_e32 v59, v60, v60
	v_fmac_f32_e32 v59, 4.0, v58
	v_sqrt_f32_e32 v59, v59
	v_mul_f32_e32 v63, v62, v41
	v_mul_f32_e32 v43, v62, v40
	v_fma_f32 v40, v61, v40, -v63
	v_fma_f32 v41, v61, v41, v43
	v_add_f32_e64 v59, |v60|, v59
	v_add_f32_e32 v59, 0x0da24260, v59
	v_rcp_f32_e32 v59, v59
	v_add_f32_e32 v58, v57, v57
	v_mul_f32_e32 v59, v58, v59
	v_cndmask_b32_e64 v59, v59, -v59, vcc
	v_fma_f32 v58, v59, v59, 1.0
	v_rsq_f32_e32 v61, v58
	s_nop 0
	v_mul_f32_e32 v62, v61, v59
	v_mul_f32_e32 v55, v62, v54
	v_mul_f32_e32 v56, v62, v52
	v_fma_f32 v52, v61, v52, -v55
	v_fma_f32 v54, v61, v54, v56
	v_mul_f32_e32 v55, v53, v53
	v_mul_f32_e32 v56, v54, v54
	v_mul_f32_e32 v57, v53, v54
	v_add_f32_dpp v55, v55, v55 quad_perm:[1,0,3,2] row_mask:0xf bank_mask:0xf
	v_add_f32_dpp v56, v56, v56 quad_perm:[1,0,3,2] row_mask:0xf bank_mask:0xf
	v_add_f32_dpp v57, v57, v57 quad_perm:[1,0,3,2] row_mask:0xf bank_mask:0xf
	v_add_f32_dpp v55, v55, v55 quad_perm:[2,3,0,1] row_mask:0xf bank_mask:0xf
	v_add_f32_dpp v56, v56, v56 quad_perm:[2,3,0,1] row_mask:0xf bank_mask:0xf
	v_add_f32_dpp v57, v57, v57 quad_perm:[2,3,0,1] row_mask:0xf bank_mask:0xf
	v_sub_f32_e32 v60, v56, v55
	v_mul_f32_e32 v58, v57, v57
	v_cmp_gt_f32_e32 vcc, 0, v60
	v_mul_f32_e32 v59, v60, v60
	v_fmac_f32_e32 v59, 4.0, v58
	v_sqrt_f32_e32 v59, v59
	v_mul_f32_e32 v63, v62, v42
	v_mul_f32_e32 v43, v62, v40
	v_fma_f32 v40, v61, v40, -v63
	v_fma_f32 v42, v61, v42, v43
	v_add_f32_e64 v59, |v60|, v59
	v_add_f32_e32 v59, 0x0da24260, v59
	v_rcp_f32_e32 v59, v59
	v_add_f32_e32 v58, v57, v57
	v_mul_f32_e32 v59, v58, v59
	v_cndmask_b32_e64 v59, v59, -v59, vcc
	v_fma_f32 v58, v59, v59, 1.0
	v_rsq_f32_e32 v61, v58
	s_nop 0
	v_mul_f32_e32 v62, v61, v59
	v_mul_f32_e32 v55, v62, v54
	v_mul_f32_e32 v56, v62, v53
	v_fma_f32 v53, v61, v53, -v55
	v_fma_f32 v54, v61, v54, v56
	v_mul_f32_e32 v55, v52, v52
	v_mul_f32_e32 v56, v53, v53
	v_mul_f32_e32 v57, v52, v53
	v_add_f32_dpp v55, v55, v55 quad_perm:[1,0,3,2] row_mask:0xf bank_mask:0xf
	v_add_f32_dpp v56, v56, v56 quad_perm:[1,0,3,2] row_mask:0xf bank_mask:0xf
	v_add_f32_dpp v57, v57, v57 quad_perm:[1,0,3,2] row_mask:0xf bank_mask:0xf
	v_add_f32_dpp v55, v55, v55 quad_perm:[2,3,0,1] row_mask:0xf bank_mask:0xf
	v_add_f32_dpp v56, v56, v56 quad_perm:[2,3,0,1] row_mask:0xf bank_mask:0xf
	v_add_f32_dpp v57, v57, v57 quad_perm:[2,3,0,1] row_mask:0xf bank_mask:0xf
	v_sub_f32_e32 v60, v56, v55
	v_mul_f32_e32 v58, v57, v57
	v_cmp_gt_f32_e32 vcc, 0, v60
	v_mul_f32_e32 v59, v60, v60
	v_fmac_f32_e32 v59, 4.0, v58
	v_sqrt_f32_e32 v59, v59
	v_mul_f32_e32 v63, v62, v42
	v_mul_f32_e32 v43, v62, v41
	v_fma_f32 v41, v61, v41, -v63
	v_fma_f32 v42, v61, v42, v43
	v_add_f32_e64 v59, |v60|, v59
	v_add_f32_e32 v59, 0x0da24260, v59
	v_rcp_f32_e32 v59, v59
	v_add_f32_e32 v58, v57, v57
	v_mul_f32_e32 v59, v58, v59
	v_cndmask_b32_e64 v59, v59, -v59, vcc
	v_fma_f32 v58, v59, v59, 1.0
	v_rsq_f32_e32 v61, v58
	s_nop 0
	v_mul_f32_e32 v62, v61, v59
	v_mul_f32_e32 v55, v62, v53
	v_mul_f32_e32 v56, v62, v52
	v_fma_f32 v52, v61, v52, -v55
	v_fma_f32 v53, v61, v53, v56
	v_mul_f32_e32 v55, v52, v52
	v_mul_f32_e32 v56, v54, v54
	v_mul_f32_e32 v57, v52, v54
	v_add_f32_dpp v55, v55, v55 quad_perm:[1,0,3,2] row_mask:0xf bank_mask:0xf
	v_add_f32_dpp v56, v56, v56 quad_perm:[1,0,3,2] row_mask:0xf bank_mask:0xf
	v_add_f32_dpp v57, v57, v57 quad_perm:[1,0,3,2] row_mask:0xf bank_mask:0xf
	v_add_f32_dpp v55, v55, v55 quad_perm:[2,3,0,1] row_mask:0xf bank_mask:0xf
	v_add_f32_dpp v56, v56, v56 quad_perm:[2,3,0,1] row_mask:0xf bank_mask:0xf
	v_add_f32_dpp v57, v57, v57 quad_perm:[2,3,0,1] row_mask:0xf bank_mask:0xf
	v_sub_f32_e32 v60, v56, v55
	v_mul_f32_e32 v58, v57, v57
	v_cmp_gt_f32_e32 vcc, 0, v60
	v_mul_f32_e32 v59, v60, v60
	v_fmac_f32_e32 v59, 4.0, v58
	v_sqrt_f32_e32 v59, v59
	v_mul_f32_e32 v63, v62, v41
	v_mul_f32_e32 v43, v62, v40
	v_fma_f32 v40, v61, v40, -v63
	v_fma_f32 v41, v61, v41, v43
	v_add_f32_e64 v59, |v60|, v59
	v_add_f32_e32 v59, 0x0da24260, v59
	v_rcp_f32_e32 v59, v59
	v_add_f32_e32 v58, v57, v57
	v_mul_f32_e32 v59, v58, v59
	v_cndmask_b32_e64 v59, v59, -v59, vcc
	v_fma_f32 v58, v59, v59, 1.0
	v_rsq_f32_e32 v61, v58
	s_nop 0
	v_mul_f32_e32 v62, v61, v59
	v_mul_f32_e32 v55, v62, v54
	v_mul_f32_e32 v56, v62, v52
	v_fma_f32 v52, v61, v52, -v55
	v_fma_f32 v54, v61, v54, v56
	v_mul_f32_e32 v55, v53, v53
	v_mul_f32_e32 v56, v54, v54
	v_mul_f32_e32 v57, v53, v54
	v_add_f32_dpp v55, v55, v55 quad_perm:[1,0,3,2] row_mask:0xf bank_mask:0xf
	v_add_f32_dpp v56, v56, v56 quad_perm:[1,0,3,2] row_mask:0xf bank_mask:0xf
	v_add_f32_dpp v57, v57, v57 quad_perm:[1,0,3,2] row_mask:0xf bank_mask:0xf
	v_add_f32_dpp v55, v55, v55 quad_perm:[2,3,0,1] row_mask:0xf bank_mask:0xf
	v_add_f32_dpp v56, v56, v56 quad_perm:[2,3,0,1] row_mask:0xf bank_mask:0xf
	v_add_f32_dpp v57, v57, v57 quad_perm:[2,3,0,1] row_mask:0xf bank_mask:0xf
	v_sub_f32_e32 v60, v56, v55
	v_mul_f32_e32 v58, v57, v57
	v_cmp_gt_f32_e32 vcc, 0, v60
	v_mul_f32_e32 v59, v60, v60
	v_fmac_f32_e32 v59, 4.0, v58
	v_sqrt_f32_e32 v59, v59
	v_mul_f32_e32 v63, v62, v42
	v_mul_f32_e32 v43, v62, v40
	v_fma_f32 v40, v61, v40, -v63
	v_fma_f32 v42, v61, v42, v43
	v_add_f32_e64 v59, |v60|, v59
	v_add_f32_e32 v59, 0x0da24260, v59
	v_rcp_f32_e32 v59, v59
	v_add_f32_e32 v58, v57, v57
	v_mul_f32_e32 v59, v58, v59
	v_cndmask_b32_e64 v59, v59, -v59, vcc
	v_fma_f32 v58, v59, v59, 1.0
	v_rsq_f32_e32 v61, v58
	s_nop 0
	v_mul_f32_e32 v62, v61, v59
	v_mul_f32_e32 v55, v62, v54
	v_mul_f32_e32 v56, v62, v53
	v_fma_f32 v53, v61, v53, -v55
	v_fma_f32 v54, v61, v54, v56
	v_mul_f32_e32 v55, v52, v52
	v_mul_f32_e32 v56, v53, v53
	v_mul_f32_e32 v57, v52, v53
	v_add_f32_dpp v55, v55, v55 quad_perm:[1,0,3,2] row_mask:0xf bank_mask:0xf
	v_add_f32_dpp v56, v56, v56 quad_perm:[1,0,3,2] row_mask:0xf bank_mask:0xf
	v_add_f32_dpp v57, v57, v57 quad_perm:[1,0,3,2] row_mask:0xf bank_mask:0xf
	v_add_f32_dpp v55, v55, v55 quad_perm:[2,3,0,1] row_mask:0xf bank_mask:0xf
	v_add_f32_dpp v56, v56, v56 quad_perm:[2,3,0,1] row_mask:0xf bank_mask:0xf
	v_add_f32_dpp v57, v57, v57 quad_perm:[2,3,0,1] row_mask:0xf bank_mask:0xf
	v_sub_f32_e32 v60, v56, v55
	v_mul_f32_e32 v58, v57, v57
	v_cmp_gt_f32_e32 vcc, 0, v60
	v_mul_f32_e32 v59, v60, v60
	v_fmac_f32_e32 v59, 4.0, v58
	v_sqrt_f32_e32 v59, v59
	v_mul_f32_e32 v63, v62, v42
	v_mul_f32_e32 v43, v62, v41
	v_fma_f32 v41, v61, v41, -v63
	v_fma_f32 v42, v61, v42, v43
	v_add_f32_e64 v59, |v60|, v59
	v_add_f32_e32 v59, 0x0da24260, v59
	v_rcp_f32_e32 v59, v59
	v_add_f32_e32 v58, v57, v57
	v_mul_f32_e32 v59, v58, v59
	v_cndmask_b32_e64 v59, v59, -v59, vcc
	v_fma_f32 v58, v59, v59, 1.0
	v_rsq_f32_e32 v61, v58
	s_nop 0
	v_mul_f32_e32 v62, v61, v59
	v_mul_f32_e32 v55, v62, v53
	v_mul_f32_e32 v56, v62, v52
	v_fma_f32 v52, v61, v52, -v55
	v_fma_f32 v53, v61, v53, v56
	v_mul_f32_e32 v55, v52, v52
	v_mul_f32_e32 v56, v54, v54
	v_mul_f32_e32 v57, v52, v54
	v_add_f32_dpp v55, v55, v55 quad_perm:[1,0,3,2] row_mask:0xf bank_mask:0xf
	v_add_f32_dpp v56, v56, v56 quad_perm:[1,0,3,2] row_mask:0xf bank_mask:0xf
	v_add_f32_dpp v57, v57, v57 quad_perm:[1,0,3,2] row_mask:0xf bank_mask:0xf
	v_add_f32_dpp v55, v55, v55 quad_perm:[2,3,0,1] row_mask:0xf bank_mask:0xf
	v_add_f32_dpp v56, v56, v56 quad_perm:[2,3,0,1] row_mask:0xf bank_mask:0xf
	v_add_f32_dpp v57, v57, v57 quad_perm:[2,3,0,1] row_mask:0xf bank_mask:0xf
	v_sub_f32_e32 v60, v56, v55
	v_mul_f32_e32 v58, v57, v57
	v_cmp_gt_f32_e32 vcc, 0, v60
	v_mul_f32_e32 v59, v60, v60
	v_fmac_f32_e32 v59, 4.0, v58
	v_sqrt_f32_e32 v59, v59
	v_mul_f32_e32 v63, v62, v41
	v_mul_f32_e32 v43, v62, v40
	v_fma_f32 v40, v61, v40, -v63
	v_fma_f32 v41, v61, v41, v43
	v_add_f32_e64 v59, |v60|, v59
	v_add_f32_e32 v59, 0x0da24260, v59
	v_rcp_f32_e32 v59, v59
	v_add_f32_e32 v58, v57, v57
	v_mul_f32_e32 v59, v58, v59
	v_cndmask_b32_e64 v59, v59, -v59, vcc
	v_fma_f32 v58, v59, v59, 1.0
	v_rsq_f32_e32 v61, v58
	s_nop 0
	v_mul_f32_e32 v62, v61, v59
	v_mul_f32_e32 v55, v62, v54
	v_mul_f32_e32 v56, v62, v52
	v_fma_f32 v52, v61, v52, -v55
	v_fma_f32 v54, v61, v54, v56
	v_mul_f32_e32 v55, v53, v53
	v_mul_f32_e32 v56, v54, v54
	v_mul_f32_e32 v57, v53, v54
	v_add_f32_dpp v55, v55, v55 quad_perm:[1,0,3,2] row_mask:0xf bank_mask:0xf
	v_add_f32_dpp v56, v56, v56 quad_perm:[1,0,3,2] row_mask:0xf bank_mask:0xf
	v_add_f32_dpp v57, v57, v57 quad_perm:[1,0,3,2] row_mask:0xf bank_mask:0xf
	v_add_f32_dpp v55, v55, v55 quad_perm:[2,3,0,1] row_mask:0xf bank_mask:0xf
	v_add_f32_dpp v56, v56, v56 quad_perm:[2,3,0,1] row_mask:0xf bank_mask:0xf
	v_add_f32_dpp v57, v57, v57 quad_perm:[2,3,0,1] row_mask:0xf bank_mask:0xf
	v_sub_f32_e32 v60, v56, v55
	v_mul_f32_e32 v58, v57, v57
	v_cmp_gt_f32_e32 vcc, 0, v60
	v_mul_f32_e32 v59, v60, v60
	v_fmac_f32_e32 v59, 4.0, v58
	v_sqrt_f32_e32 v59, v59
	v_mul_f32_e32 v63, v62, v42
	v_mul_f32_e32 v43, v62, v40
	v_fma_f32 v40, v61, v40, -v63
	v_fma_f32 v42, v61, v42, v43
	v_add_f32_e64 v59, |v60|, v59
	v_add_f32_e32 v59, 0x0da24260, v59
	v_rcp_f32_e32 v59, v59
	v_add_f32_e32 v58, v57, v57
	v_mul_f32_e32 v59, v58, v59
	v_cndmask_b32_e64 v59, v59, -v59, vcc
	v_fma_f32 v58, v59, v59, 1.0
	v_rsq_f32_e32 v61, v58
	s_nop 0
	v_mul_f32_e32 v62, v61, v59
	v_mul_f32_e32 v55, v62, v54
	v_mul_f32_e32 v56, v62, v53
	v_fma_f32 v53, v61, v53, -v55
	v_fma_f32 v54, v61, v54, v56
	v_mul_f32_e32 v63, v62, v42
	v_mul_f32_e32 v43, v62, v41
	v_fma_f32 v41, v61, v41, -v63
	v_fma_f32 v42, v61, v42, v43
	v_mul_f32_e32 v55, v52, v52
	v_mul_f32_e32 v56, v53, v53
	v_mul_f32_e32 v57, v54, v54
	v_add_f32_dpp v55, v55, v55 quad_perm:[1,0,3,2] row_mask:0xf bank_mask:0xf
	v_add_f32_dpp v56, v56, v56 quad_perm:[1,0,3,2] row_mask:0xf bank_mask:0xf
	v_add_f32_dpp v57, v57, v57 quad_perm:[1,0,3,2] row_mask:0xf bank_mask:0xf
	v_add_f32_dpp v55, v55, v55 quad_perm:[2,3,0,1] row_mask:0xf bank_mask:0xf
	v_add_f32_dpp v56, v56, v56 quad_perm:[2,3,0,1] row_mask:0xf bank_mask:0xf
	v_add_f32_dpp v57, v57, v57 quad_perm:[2,3,0,1] row_mask:0xf bank_mask:0xf
	v_cmp_le_f32_e64 s[28:29], v55, v56
	v_cmp_le_f32_e64 s[30:31], v55, v57
	v_cmp_lt_f32_e32 vcc, v57, v56
	s_and_b64 s[28:29], s[28:29], s[30:31]
	s_andn2_b64 s[30:31], vcc, s[28:29]
	v_cndmask_b32_e64 v44, v52, v53, s[28:29]
	v_cndmask_b32_e64 v45, v54, v53, s[30:31]
	v_cndmask_b32_e64 v46, v40, v41, s[28:29]
	v_cndmask_b32_e64 v47, v42, v41, s[30:31]
	v_mul_f32_e32 v58, v44, v44
	s_nop 1
	v_add_f32_dpp v58, v58, v58 quad_perm:[1,0,3,2] row_mask:0xf bank_mask:0xf
	s_nop 1
	v_add_f32_dpp v58, v58, v58 quad_perm:[2,3,0,1] row_mask:0xf bank_mask:0xf
	v_max_f32_e32 v58, 0x3aa2425, v58
	v_rsq_f32_e32 v58, v58
	s_nop 0
	v_mul_f32_e32 v48, v44, v58
	v_mul_f32_e32 v59, v48, v45
	s_nop 1
	v_add_f32_dpp v59, v59, v59 quad_perm:[1,0,3,2] row_mask:0xf bank_mask:0xf
	s_nop 1
	v_add_f32_dpp v59, v59, v59 quad_perm:[2,3,0,1] row_mask:0xf bank_mask:0xf
	v_fma_f32 v49, -v59, v48, v45
	v_mul_f32_e32 v58, v49, v49
	s_nop 1
	v_add_f32_dpp v58, v58, v58 quad_perm:[1,0,3,2] row_mask:0xf bank_mask:0xf
	s_nop 1
	v_add_f32_dpp v58, v58, v58 quad_perm:[2,3,0,1] row_mask:0xf bank_mask:0xf
	v_max_f32_e32 v58, 0x3aa2425, v58
	v_rsq_f32_e32 v58, v58
	s_nop 0
	v_mul_f32_e32 v50, v49, v58
	v_mov_b32_dpp v43, v47 quad_perm:[2,0,1,3] row_mask:0xf bank_mask:0xf
	v_mov_b32_dpp v63, v47 quad_perm:[1,2,0,3] row_mask:0xf bank_mask:0xf
	v_mov_b32_dpp v62, v50 quad_perm:[2,0,1,3] row_mask:0xf bank_mask:0xf
	v_mov_b32_dpp v61, v50 quad_perm:[1,2,0,3] row_mask:0xf bank_mask:0xf
	v_mul_f32_dpp v60, v46, v43 quad_perm:[1,2,0,3] row_mask:0xf bank_mask:0xf
	v_mul_f32_dpp v51, v48, v62 quad_perm:[1,2,0,3] row_mask:0xf bank_mask:0xf
	s_nop 0
	v_fmac_f32_dpp v60, -v46, v63 quad_perm:[2,0,1,3] row_mask:0xf bank_mask:0xf
	v_fmac_f32_dpp v51, -v48, v61 quad_perm:[2,0,1,3] row_mask:0xf bank_mask:0xf
	v_mul_f32_dpp v52, v46, v48 quad_perm:[0,0,0,0] row_mask:0xf bank_mask:0xf
	v_mul_f32_dpp v53, v46, v48 quad_perm:[1,1,1,1] row_mask:0xf bank_mask:0xf
	v_mul_f32_dpp v54, v46, v48 quad_perm:[2,2,2,2] row_mask:0xf bank_mask:0xf
	v_fmac_f32_dpp v52, v47, v50 quad_perm:[0,0,0,0] row_mask:0xf bank_mask:0xf
	v_fmac_f32_dpp v53, v47, v50 quad_perm:[1,1,1,1] row_mask:0xf bank_mask:0xf
	v_fmac_f32_dpp v54, v47, v50 quad_perm:[2,2,2,2] row_mask:0xf bank_mask:0xf
	v_fmac_f32_dpp v52, v60, v51 quad_perm:[0,0,0,0] row_mask:0xf bank_mask:0xf
	v_fmac_f32_dpp v53, v60, v51 quad_perm:[1,1,1,1] row_mask:0xf bank_mask:0xf
	v_fmac_f32_dpp v54, v60, v51 quad_perm:[2,2,2,2] row_mask:0xf bank_mask:0xf
	v_mov_b32_e32 v55, 0
	v_writelane_b32 v55, s32, 48
	v_writelane_b32 v55, s33, 49
	v_writelane_b32 v55, s34, 50
	v_mul_f32_e32 v55, 0xbc800000, v55
	v_mul_f32_e32 v56, v55, v52
	v_mul_f32_e32 v57, v55, v53
	v_mul_f32_e32 v58, v55, v54
	v_add_f32_dpp v56, v56, v56 quad_perm:[1,0,3,2] row_mask:0xf bank_mask:0xf
	v_add_f32_dpp v57, v57, v57 quad_perm:[1,0,3,2] row_mask:0xf bank_mask:0xf
	v_add_f32_dpp v58, v58, v58 quad_perm:[1,0,3,2] row_mask:0xf bank_mask:0xf
	v_add_f32_dpp v56, v56, v56 quad_perm:[2,3,0,1] row_mask:0xf bank_mask:0xf
	v_add_f32_dpp v57, v57, v57 quad_perm:[2,3,0,1] row_mask:0xf bank_mask:0xf
	v_add_f32_dpp v58, v58, v58 quad_perm:[2,3,0,1] row_mask:0xf bank_mask:0xf
	v_cndmask_b32_e64 v52, v52, v56, s[26:27]
	v_cndmask_b32_e64 v53, v53, v57, s[26:27]
	v_cndmask_b32_e64 v54, v54, v58, s[26:27]
	v_subrev_u32_e32 v59, 48, v0
	v_lshlrev_b32_e32 v59, 4, v59
	s_mov_b32 s20, 0
	s_mov_b32 s21, 0xf0000
	s_mov_b64 exec, s[20:21]
	ds_write_b96 v59, v[52:54] offset:24576
	s_mov_b64 exec, -1
	s_waitcnt lgkmcnt(0)
	s_branch .Ljoin
.Lbulk_waves:
	s_mov_b32 m0, s18
	s_nop 0
	global_load_lds_dwordx4 v1, s[40:41] nt
	global_load_lds_dwordx4 v1, s[40:41] offset:1024 nt
	global_load_lds_dwordx4 v1, s[40:41] offset:2048 nt
	global_load_lds_dwordx4 v1, s[40:41] offset:3072 nt
	s_add_u32 m0, s18, 0x1000
	s_nop 0
	global_load_lds_dwordx4 v1, s[42:43] nt
	s_and_saveexec_b64 s[16:17], s[14:15]
	global_load_lds_dwordx4 v1, s[42:43] offset:1024 nt
	s_mov_b64 exec, s[16:17]
	s_waitcnt vmcnt(0)
	s_waitcnt lgkmcnt(0)
	s_barrier
